# v53 + G1 tail (cumulative log decay LA): 16-row inclusive prefix sums by DPP row_shr adds instead of four dependent ds_bpermute round trips per column tile (16 sites, bit-identical)
# speedup vs baseline: 1.0056x; 1.0056x over previous
; #define MFMA16(a, b, c) __builtin_amdgcn_mfma_f32_16x16x32_bf16((a), (b), (c), 0, 0, 0)
; __device__ __forceinline__ float logsig16(float x) { return ((x < 0.f ? x : 0.f) - 0.6931471805599453f * __builtin_amdgcn_logf(1.0f + __builtin_amdgcn_exp2f(-1.4426950408889634f * fabsf(x)))) * (1.0f / 16.0f); }
; template <int layer> __device__ __forceinline__ void layer_phases(const Ctx& c, unsigned char* lds) {
;     ...
;                     for (int ct = 0; ct < 8; ++ct) { const f32x4 z = MFMA16(wfr[ct], afr, ((f32x4){0.f, 0.f, 0.f, 0.f})) + bcl[ct];
;                         f32x4 v; v[0] = pg8::logsig16(z[0]); v[1] = pg8::logsig16(z[1]); v[2] = pg8::logsig16(z[2]); v[3] = pg8::logsig16(z[3]);
; #pragma unroll
;                         for (int st = 1; st < 16; st <<= 1) { f32x4 t;
; #pragma unroll
;                             for (int j = 0; j < 4; ++j) t[j] = __shfl_up(v[j], st, 16);
;                             if (ql >= st) v += t; }
;                         cv[ct] = v;
;                         if (ql == 15) *(f32x4*)(tot + rt * 256 + 16 * (8 * kh + ct) + 4 * g4) = v; }
.LBB0_269:
	s_or_b64 exec, exec, s[16:17]
	s_nop 0
	v_mfma_f32_16x16x32_bf16 v[66:69], v[2:5], v[70:73], 0
	v_and_b32_e32 v82, 0x70, v228
	v_add_u32_e32 v78, -1, v228
	v_cmp_lt_i32_e32 vcc, v78, v82
	s_nop 1
	v_cndmask_b32_e32 v78, v78, v228, vcc
	s_nop 1
	v_pk_add_f32 v[66:67], v[10:11], v[66:67]
	v_pk_add_f32 v[68:69], v[12:13], v[68:69]
	v_mul_f32_e64 v74, |v66|, s93
	v_mul_f32_e64 v75, |v67|, s93
	v_exp_f32_e32 v74, v74
	v_exp_f32_e32 v75, v75
	v_mul_f32_e64 v76, |v68|, s93
	v_mul_f32_e64 v77, |v69|, s93
	v_add_f32_e32 v74, 1.0, v74
	v_add_f32_e32 v75, 1.0, v75
	v_log_f32_e32 v74, v74
	v_log_f32_e32 v75, v75
	v_exp_f32_e32 v76, v76
	v_exp_f32_e32 v77, v77
	v_min_f32_e32 v67, 0, v67
	v_min_f32_e32 v66, 0, v66
	v_pk_fma_f32 v[66:67], v[74:75], s[64:65], v[66:67] op_sel_hi:[1,0,1] neg_lo:[1,0,0] neg_hi:[1,0,0]
	v_add_f32_e32 v74, 1.0, v76
	v_add_f32_e32 v75, 1.0, v77
	v_log_f32_e32 v74, v74
	v_log_f32_e32 v75, v75
	v_min_f32_e32 v69, 0, v69
	v_min_f32_e32 v68, 0, v68
	v_lshlrev_b32_e32 v98, 2, v78
	v_pk_fma_f32 v[68:69], v[74:75], s[64:65], v[68:69] op_sel_hi:[1,0,1] neg_lo:[1,0,0] neg_hi:[1,0,0]
	v_add_u32_e32 v74, -2, v228
	v_cmp_lt_i32_e32 vcc, v74, v82
	v_cndmask_b32_e32 v74, v74, v228, vcc
	v_lshlrev_b32_e32 v99, 2, v74
	v_add_u32_e32 v74, -4, v228
	v_cmp_lt_i32_e32 vcc, v74, v82
	v_cndmask_b32_e32 v74, v74, v228, vcc
	v_lshlrev_b32_e32 v100, 2, v74
	v_add_u32_e32 v74, -8, v228
	v_cmp_lt_i32_e32 vcc, v74, v82
	v_cndmask_b32_e32 v74, v74, v228, vcc
	v_lshlrev_b32_e32 v101, 2, v74
	v_pk_mul_f32 v[66:67], v[66:67], s[66:67] op_sel_hi:[1,0]
	v_pk_mul_f32 v[68:69], v[68:69], s[66:67] op_sel_hi:[1,0]
	s_nop 1
	v_add_f32_dpp v66, v66, v66 row_shr:1 row_mask:0xf bank_mask:0xf
	v_add_f32_dpp v67, v67, v67 row_shr:1 row_mask:0xf bank_mask:0xf
	v_add_f32_dpp v68, v68, v68 row_shr:1 row_mask:0xf bank_mask:0xf
	v_add_f32_dpp v69, v69, v69 row_shr:1 row_mask:0xf bank_mask:0xf
	v_add_f32_dpp v66, v66, v66 row_shr:2 row_mask:0xf bank_mask:0xf
	v_add_f32_dpp v67, v67, v67 row_shr:2 row_mask:0xf bank_mask:0xf
	v_add_f32_dpp v68, v68, v68 row_shr:2 row_mask:0xf bank_mask:0xf
	v_add_f32_dpp v69, v69, v69 row_shr:2 row_mask:0xf bank_mask:0xf
	v_add_f32_dpp v66, v66, v66 row_shr:4 row_mask:0xf bank_mask:0xf
	v_add_f32_dpp v67, v67, v67 row_shr:4 row_mask:0xf bank_mask:0xf
	v_add_f32_dpp v68, v68, v68 row_shr:4 row_mask:0xf bank_mask:0xf
	v_add_f32_dpp v69, v69, v69 row_shr:4 row_mask:0xf bank_mask:0xf
	v_add_f32_dpp v66, v66, v66 row_shr:8 row_mask:0xf bank_mask:0xf
	v_add_f32_dpp v67, v67, v67 row_shr:8 row_mask:0xf bank_mask:0xf
	v_add_f32_dpp v68, v68, v68 row_shr:8 row_mask:0xf bank_mask:0xf
	v_add_f32_dpp v69, v69, v69 row_shr:8 row_mask:0xf bank_mask:0xf
	s_and_saveexec_b64 s[16:17], s[6:7]
	v_add_u32_e32 v74, s3, v107
	ds_write_b128 v74, v[66:69] offset:8192
	s_or_b64 exec, exec, s[16:17]
	v_mfma_f32_16x16x32_bf16 v[74:77], v[6:9], v[70:73], 0
	s_nop 7
	v_pk_add_f32 v[74:75], v[14:15], v[74:75]
	v_pk_add_f32 v[76:77], v[16:17], v[76:77]
	v_mul_f32_e64 v78, |v74|, s93
	v_mul_f32_e64 v79, |v75|, s93
	v_exp_f32_e32 v78, v78
	v_exp_f32_e32 v79, v79
	v_mul_f32_e64 v80, |v76|, s93
	v_mul_f32_e64 v81, |v77|, s93
	v_add_f32_e32 v78, 1.0, v78
	v_add_f32_e32 v79, 1.0, v79
	v_log_f32_e32 v78, v78
	v_log_f32_e32 v79, v79
	v_exp_f32_e32 v80, v80
	v_exp_f32_e32 v81, v81
	v_min_f32_e32 v75, 0, v75
	v_min_f32_e32 v74, 0, v74
	v_pk_fma_f32 v[74:75], v[78:79], s[64:65], v[74:75] op_sel_hi:[1,0,1] neg_lo:[1,0,0] neg_hi:[1,0,0]
	v_add_f32_e32 v78, 1.0, v80
	v_add_f32_e32 v79, 1.0, v81
	v_log_f32_e32 v78, v78
	v_log_f32_e32 v79, v79
	v_min_f32_e32 v77, 0, v77
	v_min_f32_e32 v76, 0, v76
	v_pk_fma_f32 v[76:77], v[78:79], s[64:65], v[76:77] op_sel_hi:[1,0,1] neg_lo:[1,0,0] neg_hi:[1,0,0]
	v_pk_mul_f32 v[74:75], v[74:75], s[66:67] op_sel_hi:[1,0]
	v_pk_mul_f32 v[76:77], v[76:77], s[66:67] op_sel_hi:[1,0]
	s_nop 1
	v_add_f32_dpp v74, v74, v74 row_shr:1 row_mask:0xf bank_mask:0xf
	v_add_f32_dpp v75, v75, v75 row_shr:1 row_mask:0xf bank_mask:0xf
	v_add_f32_dpp v76, v76, v76 row_shr:1 row_mask:0xf bank_mask:0xf
	v_add_f32_dpp v77, v77, v77 row_shr:1 row_mask:0xf bank_mask:0xf
	v_add_f32_dpp v74, v74, v74 row_shr:2 row_mask:0xf bank_mask:0xf
	v_add_f32_dpp v75, v75, v75 row_shr:2 row_mask:0xf bank_mask:0xf
	v_add_f32_dpp v76, v76, v76 row_shr:2 row_mask:0xf bank_mask:0xf
	v_add_f32_dpp v77, v77, v77 row_shr:2 row_mask:0xf bank_mask:0xf
	v_add_f32_dpp v74, v74, v74 row_shr:4 row_mask:0xf bank_mask:0xf
	v_add_f32_dpp v75, v75, v75 row_shr:4 row_mask:0xf bank_mask:0xf
	v_add_f32_dpp v76, v76, v76 row_shr:4 row_mask:0xf bank_mask:0xf
	v_add_f32_dpp v77, v77, v77 row_shr:4 row_mask:0xf bank_mask:0xf
	v_add_f32_dpp v74, v74, v74 row_shr:8 row_mask:0xf bank_mask:0xf
	v_add_f32_dpp v75, v75, v75 row_shr:8 row_mask:0xf bank_mask:0xf
	v_add_f32_dpp v76, v76, v76 row_shr:8 row_mask:0xf bank_mask:0xf
	v_add_f32_dpp v77, v77, v77 row_shr:8 row_mask:0xf bank_mask:0xf
	s_and_saveexec_b64 s[16:17], s[6:7]
	v_add_u32_e32 v78, s80, v107
	ds_write_b128 v78, v[74:77] offset:8192
	s_or_b64 exec, exec, s[16:17]
	v_mfma_f32_16x16x32_bf16 v[78:81], v[18:21], v[70:73], 0
	s_nop 7
	v_pk_add_f32 v[78:79], v[26:27], v[78:79]
	v_pk_add_f32 v[80:81], v[28:29], v[80:81]
	v_mul_f32_e64 v82, |v78|, s93
	v_mul_f32_e64 v83, |v79|, s93
	v_exp_f32_e32 v82, v82
	v_exp_f32_e32 v83, v83
	v_mul_f32_e64 v84, |v80|, s93
	v_mul_f32_e64 v85, |v81|, s93
	v_add_f32_e32 v82, 1.0, v82
	v_add_f32_e32 v83, 1.0, v83
	v_log_f32_e32 v82, v82
	v_log_f32_e32 v83, v83
	v_exp_f32_e32 v84, v84
	v_exp_f32_e32 v85, v85
	v_min_f32_e32 v79, 0, v79
	v_min_f32_e32 v78, 0, v78
	v_pk_fma_f32 v[78:79], v[82:83], s[64:65], v[78:79] op_sel_hi:[1,0,1] neg_lo:[1,0,0] neg_hi:[1,0,0]
; #define MFMA16(a, b, c) __builtin_amdgcn_mfma_f32_16x16x32_bf16((a), (b), (c), 0, 0, 0)
; __device__ __forceinline__ float logsig16(float x) { return ((x < 0.f ? x : 0.f) - 0.6931471805599453f * __builtin_amdgcn_logf(1.0f + __builtin_amdgcn_exp2f(-1.4426950408889634f * fabsf(x)))) * (1.0f / 16.0f); }
; template <int layer> __device__ __forceinline__ void layer_phases(const Ctx& c, unsigned char* lds) {
;     ...
;                     for (int ct = 0; ct < 8; ++ct) { const f32x4 z = MFMA16(wfr[ct], afr, ((f32x4){0.f, 0.f, 0.f, 0.f})) + bcl[ct];
;                         f32x4 v; v[0] = pg8::logsig16(z[0]); v[1] = pg8::logsig16(z[1]); v[2] = pg8::logsig16(z[2]); v[3] = pg8::logsig16(z[3]);
; #pragma unroll
;                         for (int st = 1; st < 16; st <<= 1) { f32x4 t;
; #pragma unroll
;                             for (int j = 0; j < 4; ++j) t[j] = __shfl_up(v[j], st, 16);
;                             if (ql >= st) v += t; }
;                         cv[ct] = v;
;                         if (ql == 15) *(f32x4*)(tot + rt * 256 + 16 * (8 * kh + ct) + 4 * g4) = v; }
	v_add_f32_e32 v82, 1.0, v84
	v_add_f32_e32 v83, 1.0, v85
	v_log_f32_e32 v82, v82
	v_log_f32_e32 v83, v83
	v_min_f32_e32 v81, 0, v81
	v_min_f32_e32 v80, 0, v80
	v_pk_fma_f32 v[80:81], v[82:83], s[64:65], v[80:81] op_sel_hi:[1,0,1] neg_lo:[1,0,0] neg_hi:[1,0,0]
	v_pk_mul_f32 v[78:79], v[78:79], s[66:67] op_sel_hi:[1,0]
	v_pk_mul_f32 v[80:81], v[80:81], s[66:67] op_sel_hi:[1,0]
	s_nop 1
	v_add_f32_dpp v78, v78, v78 row_shr:1 row_mask:0xf bank_mask:0xf
	v_add_f32_dpp v79, v79, v79 row_shr:1 row_mask:0xf bank_mask:0xf
	v_add_f32_dpp v80, v80, v80 row_shr:1 row_mask:0xf bank_mask:0xf
	v_add_f32_dpp v81, v81, v81 row_shr:1 row_mask:0xf bank_mask:0xf
	v_add_f32_dpp v78, v78, v78 row_shr:2 row_mask:0xf bank_mask:0xf
	v_add_f32_dpp v79, v79, v79 row_shr:2 row_mask:0xf bank_mask:0xf
	v_add_f32_dpp v80, v80, v80 row_shr:2 row_mask:0xf bank_mask:0xf
	v_add_f32_dpp v81, v81, v81 row_shr:2 row_mask:0xf bank_mask:0xf
	v_add_f32_dpp v78, v78, v78 row_shr:4 row_mask:0xf bank_mask:0xf
	v_add_f32_dpp v79, v79, v79 row_shr:4 row_mask:0xf bank_mask:0xf
	v_add_f32_dpp v80, v80, v80 row_shr:4 row_mask:0xf bank_mask:0xf
	v_add_f32_dpp v81, v81, v81 row_shr:4 row_mask:0xf bank_mask:0xf
	v_add_f32_dpp v78, v78, v78 row_shr:8 row_mask:0xf bank_mask:0xf
	v_add_f32_dpp v79, v79, v79 row_shr:8 row_mask:0xf bank_mask:0xf
	v_add_f32_dpp v80, v80, v80 row_shr:8 row_mask:0xf bank_mask:0xf
	v_add_f32_dpp v81, v81, v81 row_shr:8 row_mask:0xf bank_mask:0xf
	s_and_saveexec_b64 s[16:17], s[6:7]
	v_add_u32_e32 v82, s81, v107
	ds_write_b128 v82, v[78:81] offset:8192
	s_or_b64 exec, exec, s[16:17]
	v_mfma_f32_16x16x32_bf16 v[82:85], v[22:25], v[70:73], 0
	s_nop 7
	v_pk_add_f32 v[82:83], v[30:31], v[82:83]
	v_pk_add_f32 v[84:85], v[32:33], v[84:85]
	v_mul_f32_e64 v86, |v82|, s93
	v_mul_f32_e64 v87, |v83|, s93
	v_exp_f32_e32 v86, v86
	v_exp_f32_e32 v87, v87
	v_mul_f32_e64 v88, |v84|, s93
	v_mul_f32_e64 v89, |v85|, s93
	v_add_f32_e32 v86, 1.0, v86
	v_add_f32_e32 v87, 1.0, v87
	v_log_f32_e32 v86, v86
	v_log_f32_e32 v87, v87
	v_exp_f32_e32 v88, v88
	v_exp_f32_e32 v89, v89
	v_min_f32_e32 v83, 0, v83
	v_min_f32_e32 v82, 0, v82
	v_pk_fma_f32 v[82:83], v[86:87], s[64:65], v[82:83] op_sel_hi:[1,0,1] neg_lo:[1,0,0] neg_hi:[1,0,0]
	v_add_f32_e32 v86, 1.0, v88
	v_add_f32_e32 v87, 1.0, v89
	v_log_f32_e32 v86, v86
	v_log_f32_e32 v87, v87
	v_min_f32_e32 v85, 0, v85
	v_min_f32_e32 v84, 0, v84
	v_pk_fma_f32 v[84:85], v[86:87], s[64:65], v[84:85] op_sel_hi:[1,0,1] neg_lo:[1,0,0] neg_hi:[1,0,0]
	v_pk_mul_f32 v[82:83], v[82:83], s[66:67] op_sel_hi:[1,0]
	v_pk_mul_f32 v[84:85], v[84:85], s[66:67] op_sel_hi:[1,0]
	s_nop 1
	v_add_f32_dpp v82, v82, v82 row_shr:1 row_mask:0xf bank_mask:0xf
	v_add_f32_dpp v83, v83, v83 row_shr:1 row_mask:0xf bank_mask:0xf
	v_add_f32_dpp v84, v84, v84 row_shr:1 row_mask:0xf bank_mask:0xf
	v_add_f32_dpp v85, v85, v85 row_shr:1 row_mask:0xf bank_mask:0xf
	v_add_f32_dpp v82, v82, v82 row_shr:2 row_mask:0xf bank_mask:0xf
	v_add_f32_dpp v83, v83, v83 row_shr:2 row_mask:0xf bank_mask:0xf
	v_add_f32_dpp v84, v84, v84 row_shr:2 row_mask:0xf bank_mask:0xf
	v_add_f32_dpp v85, v85, v85 row_shr:2 row_mask:0xf bank_mask:0xf
	v_add_f32_dpp v82, v82, v82 row_shr:4 row_mask:0xf bank_mask:0xf
	v_add_f32_dpp v83, v83, v83 row_shr:4 row_mask:0xf bank_mask:0xf
	v_add_f32_dpp v84, v84, v84 row_shr:4 row_mask:0xf bank_mask:0xf
	v_add_f32_dpp v85, v85, v85 row_shr:4 row_mask:0xf bank_mask:0xf
	v_add_f32_dpp v82, v82, v82 row_shr:8 row_mask:0xf bank_mask:0xf
	v_add_f32_dpp v83, v83, v83 row_shr:8 row_mask:0xf bank_mask:0xf
	v_add_f32_dpp v84, v84, v84 row_shr:8 row_mask:0xf bank_mask:0xf
	v_add_f32_dpp v85, v85, v85 row_shr:8 row_mask:0xf bank_mask:0xf
	s_and_saveexec_b64 s[16:17], s[6:7]
	v_add_u32_e32 v86, s82, v107
	ds_write_b128 v86, v[82:85] offset:8192
	s_or_b64 exec, exec, s[16:17]
	v_mfma_f32_16x16x32_bf16 v[86:89], v[34:37], v[70:73], 0
	s_nop 7
	v_pk_add_f32 v[86:87], v[42:43], v[86:87]
	v_pk_add_f32 v[88:89], v[44:45], v[88:89]
	v_mul_f32_e64 v90, |v86|, s93
	v_mul_f32_e64 v91, |v87|, s93
	v_exp_f32_e32 v90, v90
	v_exp_f32_e32 v91, v91
	v_mul_f32_e64 v92, |v88|, s93
	v_mul_f32_e64 v93, |v89|, s93
	v_add_f32_e32 v90, 1.0, v90
	v_add_f32_e32 v91, 1.0, v91
	v_log_f32_e32 v90, v90
	v_log_f32_e32 v91, v91
	v_exp_f32_e32 v92, v92
	v_exp_f32_e32 v93, v93
	v_min_f32_e32 v87, 0, v87
	v_min_f32_e32 v86, 0, v86
	v_pk_fma_f32 v[86:87], v[90:91], s[64:65], v[86:87] op_sel_hi:[1,0,1] neg_lo:[1,0,0] neg_hi:[1,0,0]
	v_add_f32_e32 v90, 1.0, v92
	v_add_f32_e32 v91, 1.0, v93
	v_log_f32_e32 v90, v90
	v_log_f32_e32 v91, v91
	v_min_f32_e32 v89, 0, v89
	v_min_f32_e32 v88, 0, v88
	v_pk_fma_f32 v[88:89], v[90:91], s[64:65], v[88:89] op_sel_hi:[1,0,1] neg_lo:[1,0,0] neg_hi:[1,0,0]
	v_pk_mul_f32 v[86:87], v[86:87], s[66:67] op_sel_hi:[1,0]
	v_pk_mul_f32 v[88:89], v[88:89], s[66:67] op_sel_hi:[1,0]
	s_nop 1
	v_add_f32_dpp v86, v86, v86 row_shr:1 row_mask:0xf bank_mask:0xf
	v_add_f32_dpp v87, v87, v87 row_shr:1 row_mask:0xf bank_mask:0xf
	v_add_f32_dpp v88, v88, v88 row_shr:1 row_mask:0xf bank_mask:0xf
	v_add_f32_dpp v89, v89, v89 row_shr:1 row_mask:0xf bank_mask:0xf
	v_add_f32_dpp v86, v86, v86 row_shr:2 row_mask:0xf bank_mask:0xf
	v_add_f32_dpp v87, v87, v87 row_shr:2 row_mask:0xf bank_mask:0xf
	v_add_f32_dpp v88, v88, v88 row_shr:2 row_mask:0xf bank_mask:0xf
	v_add_f32_dpp v89, v89, v89 row_shr:2 row_mask:0xf bank_mask:0xf
	v_add_f32_dpp v86, v86, v86 row_shr:4 row_mask:0xf bank_mask:0xf
	v_add_f32_dpp v87, v87, v87 row_shr:4 row_mask:0xf bank_mask:0xf
	v_add_f32_dpp v88, v88, v88 row_shr:4 row_mask:0xf bank_mask:0xf
	v_add_f32_dpp v89, v89, v89 row_shr:4 row_mask:0xf bank_mask:0xf
; #define MFMA16(a, b, c) __builtin_amdgcn_mfma_f32_16x16x32_bf16((a), (b), (c), 0, 0, 0)
; __device__ __forceinline__ float logsig16(float x) { return ((x < 0.f ? x : 0.f) - 0.6931471805599453f * __builtin_amdgcn_logf(1.0f + __builtin_amdgcn_exp2f(-1.4426950408889634f * fabsf(x)))) * (1.0f / 16.0f); }
; template <int layer> __device__ __forceinline__ void layer_phases(const Ctx& c, unsigned char* lds) {
;     ...
;                     for (int ct = 0; ct < 8; ++ct) { const f32x4 z = MFMA16(wfr[ct], afr, ((f32x4){0.f, 0.f, 0.f, 0.f})) + bcl[ct];
;                         f32x4 v; v[0] = pg8::logsig16(z[0]); v[1] = pg8::logsig16(z[1]); v[2] = pg8::logsig16(z[2]); v[3] = pg8::logsig16(z[3]);
; #pragma unroll
;                         for (int st = 1; st < 16; st <<= 1) { f32x4 t;
; #pragma unroll
;                             for (int j = 0; j < 4; ++j) t[j] = __shfl_up(v[j], st, 16);
;                             if (ql >= st) v += t; }
;                         cv[ct] = v;
;                         if (ql == 15) *(f32x4*)(tot + rt * 256 + 16 * (8 * kh + ct) + 4 * g4) = v; }
	v_add_f32_dpp v86, v86, v86 row_shr:8 row_mask:0xf bank_mask:0xf
	v_add_f32_dpp v87, v87, v87 row_shr:8 row_mask:0xf bank_mask:0xf
	v_add_f32_dpp v88, v88, v88 row_shr:8 row_mask:0xf bank_mask:0xf
	v_add_f32_dpp v89, v89, v89 row_shr:8 row_mask:0xf bank_mask:0xf
	s_and_saveexec_b64 s[16:17], s[6:7]
	v_add_u32_e32 v90, s83, v107
	ds_write_b128 v90, v[86:89] offset:8192
	s_or_b64 exec, exec, s[16:17]
	v_mfma_f32_16x16x32_bf16 v[90:93], v[38:41], v[70:73], 0
	s_nop 7
	v_pk_add_f32 v[90:91], v[46:47], v[90:91]
	v_pk_add_f32 v[92:93], v[48:49], v[92:93]
	v_mul_f32_e64 v94, |v90|, s93
	v_mul_f32_e64 v95, |v91|, s93
	v_exp_f32_e32 v94, v94
	v_exp_f32_e32 v95, v95
	v_mul_f32_e64 v96, |v92|, s93
	v_mul_f32_e64 v97, |v93|, s93
	v_add_f32_e32 v94, 1.0, v94
	v_add_f32_e32 v95, 1.0, v95
	v_log_f32_e32 v94, v94
	v_log_f32_e32 v95, v95
	v_exp_f32_e32 v96, v96
	v_exp_f32_e32 v97, v97
	v_min_f32_e32 v91, 0, v91
	v_min_f32_e32 v90, 0, v90
	v_pk_fma_f32 v[90:91], v[94:95], s[64:65], v[90:91] op_sel_hi:[1,0,1] neg_lo:[1,0,0] neg_hi:[1,0,0]
	v_add_f32_e32 v94, 1.0, v96
	v_add_f32_e32 v95, 1.0, v97
	v_log_f32_e32 v94, v94
	v_log_f32_e32 v95, v95
	v_min_f32_e32 v93, 0, v93
	v_min_f32_e32 v92, 0, v92
	v_pk_fma_f32 v[92:93], v[94:95], s[64:65], v[92:93] op_sel_hi:[1,0,1] neg_lo:[1,0,0] neg_hi:[1,0,0]
	v_pk_mul_f32 v[90:91], v[90:91], s[66:67] op_sel_hi:[1,0]
	v_pk_mul_f32 v[92:93], v[92:93], s[66:67] op_sel_hi:[1,0]
	s_nop 1
	v_add_f32_dpp v90, v90, v90 row_shr:1 row_mask:0xf bank_mask:0xf
	v_add_f32_dpp v91, v91, v91 row_shr:1 row_mask:0xf bank_mask:0xf
	v_add_f32_dpp v92, v92, v92 row_shr:1 row_mask:0xf bank_mask:0xf
	v_add_f32_dpp v93, v93, v93 row_shr:1 row_mask:0xf bank_mask:0xf
	v_add_f32_dpp v90, v90, v90 row_shr:2 row_mask:0xf bank_mask:0xf
	v_add_f32_dpp v91, v91, v91 row_shr:2 row_mask:0xf bank_mask:0xf
	v_add_f32_dpp v92, v92, v92 row_shr:2 row_mask:0xf bank_mask:0xf
	v_add_f32_dpp v93, v93, v93 row_shr:2 row_mask:0xf bank_mask:0xf
	v_add_f32_dpp v90, v90, v90 row_shr:4 row_mask:0xf bank_mask:0xf
	v_add_f32_dpp v91, v91, v91 row_shr:4 row_mask:0xf bank_mask:0xf
	v_add_f32_dpp v92, v92, v92 row_shr:4 row_mask:0xf bank_mask:0xf
	v_add_f32_dpp v93, v93, v93 row_shr:4 row_mask:0xf bank_mask:0xf
	v_add_f32_dpp v90, v90, v90 row_shr:8 row_mask:0xf bank_mask:0xf
	v_add_f32_dpp v91, v91, v91 row_shr:8 row_mask:0xf bank_mask:0xf
	v_add_f32_dpp v92, v92, v92 row_shr:8 row_mask:0xf bank_mask:0xf
	v_add_f32_dpp v93, v93, v93 row_shr:8 row_mask:0xf bank_mask:0xf
	s_and_saveexec_b64 s[16:17], s[6:7]
	v_add_u32_e32 v94, s84, v107
	ds_write_b128 v94, v[90:93] offset:8192
	s_or_b64 exec, exec, s[16:17]
	v_mfma_f32_16x16x32_bf16 v[94:97], v[50:53], v[70:73], 0
	s_nop 7
	v_pk_add_f32 v[94:95], v[58:59], v[94:95]
	v_pk_add_f32 v[96:97], v[60:61], v[96:97]
	v_mul_f32_e64 v102, |v94|, s93
	v_mul_f32_e64 v103, |v95|, s93
	v_exp_f32_e32 v102, v102
	v_exp_f32_e32 v103, v103
	v_mul_f32_e64 v104, |v96|, s93
	v_mul_f32_e64 v105, |v97|, s93
	v_add_f32_e32 v102, 1.0, v102
	v_add_f32_e32 v103, 1.0, v103
	v_log_f32_e32 v102, v102
	v_log_f32_e32 v103, v103
	v_exp_f32_e32 v104, v104
	v_exp_f32_e32 v105, v105
	v_min_f32_e32 v95, 0, v95
	v_min_f32_e32 v94, 0, v94
	v_pk_fma_f32 v[94:95], v[102:103], s[64:65], v[94:95] op_sel_hi:[1,0,1] neg_lo:[1,0,0] neg_hi:[1,0,0]
	v_add_f32_e32 v102, 1.0, v104
	v_add_f32_e32 v103, 1.0, v105
	v_log_f32_e32 v102, v102
	v_log_f32_e32 v103, v103
	v_min_f32_e32 v97, 0, v97
	v_min_f32_e32 v96, 0, v96
	v_pk_fma_f32 v[96:97], v[102:103], s[64:65], v[96:97] op_sel_hi:[1,0,1] neg_lo:[1,0,0] neg_hi:[1,0,0]
	v_pk_mul_f32 v[94:95], v[94:95], s[66:67] op_sel_hi:[1,0]
	v_pk_mul_f32 v[96:97], v[96:97], s[66:67] op_sel_hi:[1,0]
	s_nop 1
	v_add_f32_dpp v94, v94, v94 row_shr:1 row_mask:0xf bank_mask:0xf
; __device__ __forceinline__ float logsig16(float x) { return ((x < 0.f ? x : 0.f) - 0.6931471805599453f * __builtin_amdgcn_logf(1.0f + __builtin_amdgcn_exp2f(-1.4426950408889634f * fabsf(x)))) * (1.0f / 16.0f); }
; #define MFMA16(a, b, c) __builtin_amdgcn_mfma_f32_16x16x32_bf16((a), (b), (c), 0, 0, 0)
; template <int layer> __device__ __forceinline__ void layer_phases(const Ctx& c, unsigned char* lds) {
;     ...
;                     for (int ct = 0; ct < 8; ++ct) { const f32x4 z = MFMA16(wfr[ct], afr, ((f32x4){0.f, 0.f, 0.f, 0.f})) + bcl[ct];
;                         f32x4 v; v[0] = pg8::logsig16(z[0]); v[1] = pg8::logsig16(z[1]); v[2] = pg8::logsig16(z[2]); v[3] = pg8::logsig16(z[3]);
; #pragma unroll
;                         for (int st = 1; st < 16; st <<= 1) { f32x4 t;
; #pragma unroll
;                             for (int j = 0; j < 4; ++j) t[j] = __shfl_up(v[j], st, 16);
;                             if (ql >= st) v += t; }
;                         cv[ct] = v;
;                         if (ql == 15) *(f32x4*)(tot + rt * 256 + 16 * (8 * kh + ct) + 4 * g4) = v; }
;                     __syncthreads();
; #pragma unroll
;                     for (int ct = 0; ct < 8; ++ct) { f32x4 v = cv[ct];
; #pragma unroll
;                         for (int r2 = 0; r2 < 3; ++r2) if (r2 < rt) v += *(const f32x4*)(tot + r2 * 256 + 16 * (8 * kh + ct) + 4 * g4);
	v_add_f32_dpp v95, v95, v95 row_shr:1 row_mask:0xf bank_mask:0xf
	v_add_f32_dpp v96, v96, v96 row_shr:1 row_mask:0xf bank_mask:0xf
	v_add_f32_dpp v97, v97, v97 row_shr:1 row_mask:0xf bank_mask:0xf
	v_add_f32_dpp v94, v94, v94 row_shr:2 row_mask:0xf bank_mask:0xf
	v_add_f32_dpp v95, v95, v95 row_shr:2 row_mask:0xf bank_mask:0xf
	v_add_f32_dpp v96, v96, v96 row_shr:2 row_mask:0xf bank_mask:0xf
	v_add_f32_dpp v97, v97, v97 row_shr:2 row_mask:0xf bank_mask:0xf
	v_add_f32_dpp v94, v94, v94 row_shr:4 row_mask:0xf bank_mask:0xf
	v_add_f32_dpp v95, v95, v95 row_shr:4 row_mask:0xf bank_mask:0xf
	v_add_f32_dpp v96, v96, v96 row_shr:4 row_mask:0xf bank_mask:0xf
	v_add_f32_dpp v97, v97, v97 row_shr:4 row_mask:0xf bank_mask:0xf
	v_add_f32_dpp v94, v94, v94 row_shr:8 row_mask:0xf bank_mask:0xf
	v_add_f32_dpp v95, v95, v95 row_shr:8 row_mask:0xf bank_mask:0xf
	v_add_f32_dpp v96, v96, v96 row_shr:8 row_mask:0xf bank_mask:0xf
	v_add_f32_dpp v97, v97, v97 row_shr:8 row_mask:0xf bank_mask:0xf
	s_and_saveexec_b64 s[16:17], s[6:7]
	v_add_u32_e32 v102, s85, v107
	ds_write_b128 v102, v[94:97] offset:8192
	s_or_b64 exec, exec, s[16:17]
	v_mfma_f32_16x16x32_bf16 v[70:73], v[54:57], v[70:73], 0
	s_nop 7
	v_pk_add_f32 v[70:71], v[62:63], v[70:71]
	v_pk_add_f32 v[72:73], v[64:65], v[72:73]
	v_mul_f32_e64 v102, |v70|, s93
	v_mul_f32_e64 v103, |v71|, s93
	v_exp_f32_e32 v102, v102
	v_exp_f32_e32 v103, v103
	v_mul_f32_e64 v104, |v72|, s93
	v_mul_f32_e64 v105, |v73|, s93
	v_add_f32_e32 v102, 1.0, v102
	v_add_f32_e32 v103, 1.0, v103
	v_log_f32_e32 v102, v102
	v_log_f32_e32 v103, v103
	v_exp_f32_e32 v104, v104
	v_exp_f32_e32 v105, v105
	v_min_f32_e32 v71, 0, v71
	v_min_f32_e32 v70, 0, v70
	v_pk_fma_f32 v[70:71], v[102:103], s[64:65], v[70:71] op_sel_hi:[1,0,1] neg_lo:[1,0,0] neg_hi:[1,0,0]
	v_add_f32_e32 v102, 1.0, v104
	v_add_f32_e32 v103, 1.0, v105
	v_log_f32_e32 v102, v102
	v_log_f32_e32 v103, v103
	v_min_f32_e32 v73, 0, v73
	v_min_f32_e32 v72, 0, v72
	v_pk_fma_f32 v[72:73], v[102:103], s[64:65], v[72:73] op_sel_hi:[1,0,1] neg_lo:[1,0,0] neg_hi:[1,0,0]
	v_pk_mul_f32 v[70:71], v[70:71], s[66:67] op_sel_hi:[1,0]
	v_pk_mul_f32 v[72:73], v[72:73], s[66:67] op_sel_hi:[1,0]
	s_nop 1
	v_add_f32_dpp v70, v70, v70 row_shr:1 row_mask:0xf bank_mask:0xf
	v_add_f32_dpp v71, v71, v71 row_shr:1 row_mask:0xf bank_mask:0xf
	v_add_f32_dpp v72, v72, v72 row_shr:1 row_mask:0xf bank_mask:0xf
	v_add_f32_dpp v73, v73, v73 row_shr:1 row_mask:0xf bank_mask:0xf
	v_add_f32_dpp v70, v70, v70 row_shr:2 row_mask:0xf bank_mask:0xf
	v_add_f32_dpp v71, v71, v71 row_shr:2 row_mask:0xf bank_mask:0xf
	v_add_f32_dpp v72, v72, v72 row_shr:2 row_mask:0xf bank_mask:0xf
	v_add_f32_dpp v73, v73, v73 row_shr:2 row_mask:0xf bank_mask:0xf
	v_add_f32_dpp v70, v70, v70 row_shr:4 row_mask:0xf bank_mask:0xf
	v_add_f32_dpp v71, v71, v71 row_shr:4 row_mask:0xf bank_mask:0xf
	v_add_f32_dpp v72, v72, v72 row_shr:4 row_mask:0xf bank_mask:0xf
	v_add_f32_dpp v73, v73, v73 row_shr:4 row_mask:0xf bank_mask:0xf
	v_add_f32_dpp v70, v70, v70 row_shr:8 row_mask:0xf bank_mask:0xf
	v_add_f32_dpp v71, v71, v71 row_shr:8 row_mask:0xf bank_mask:0xf
	v_add_f32_dpp v72, v72, v72 row_shr:8 row_mask:0xf bank_mask:0xf
	v_add_f32_dpp v73, v73, v73 row_shr:8 row_mask:0xf bank_mask:0xf
	s_and_saveexec_b64 s[16:17], s[6:7]
	v_add_u32_e32 v98, s88, v107
	ds_write_b128 v98, v[70:73] offset:8192
	s_or_b64 exec, exec, s[16:17]
	v_cndmask_b32_e64 v98, 0, 1, s[56:57]
	v_cmp_ne_u32_e64 s[16:17], 1, v98
	s_andn2_b64 vcc, exec, s[56:57]
	v_add_u32_e32 v98, s3, v144
	s_waitcnt lgkmcnt(0)
	s_barrier
	s_cbranch_vccnz .LBB0_287
	ds_read_b128 v[100:103], v98 offset:8192
	s_waitcnt lgkmcnt(0)
	v_pk_add_f32 v[68:69], v[68:69], v[102:103]
	v_pk_add_f32 v[66:67], v[66:67], v[100:101]

; #define MFMA16(a, b, c) __builtin_amdgcn_mfma_f32_16x16x32_bf16((a), (b), (c), 0, 0, 0)
; __device__ __forceinline__ float logsig16(float x) { return ((x < 0.f ? x : 0.f) - 0.6931471805599453f * __builtin_amdgcn_logf(1.0f + __builtin_amdgcn_exp2f(-1.4426950408889634f * fabsf(x)))) * (1.0f / 16.0f); }
; template <int layer> __device__ __forceinline__ void layer_phases(const Ctx& c, unsigned char* lds) {
;     ...
;                     for (int ct = 0; ct < 8; ++ct) { const f32x4 z = MFMA16(wfr[ct], afr, ((f32x4){0.f, 0.f, 0.f, 0.f})) + bcl[ct];
;                         f32x4 v; v[0] = pg8::logsig16(z[0]); v[1] = pg8::logsig16(z[1]); v[2] = pg8::logsig16(z[2]); v[3] = pg8::logsig16(z[3]);
; #pragma unroll
;                         for (int st = 1; st < 16; st <<= 1) { f32x4 t;
; #pragma unroll
;                             for (int j = 0; j < 4; ++j) t[j] = __shfl_up(v[j], st, 16);
;                             if (ql >= st) v += t; }
;                         cv[ct] = v;
;                         if (ql == 15) *(f32x4*)(tot + rt * 256 + 16 * (8 * kh + ct) + 4 * g4) = v; }
.LBB0_960:
	s_or_b64 exec, exec, s[16:17]
	s_nop 0
	v_mfma_f32_16x16x32_bf16 v[66:69], v[2:5], v[70:73], 0
	v_and_b32_e32 v82, 0x70, v228
	v_add_u32_e32 v78, -1, v228
	v_cmp_lt_i32_e32 vcc, v78, v82
	s_nop 1
	v_cndmask_b32_e32 v78, v78, v228, vcc
	s_nop 1
	v_pk_add_f32 v[66:67], v[10:11], v[66:67]
	v_pk_add_f32 v[68:69], v[12:13], v[68:69]
	v_mul_f32_e64 v74, |v66|, s84
	v_mul_f32_e64 v75, |v67|, s84
	v_exp_f32_e32 v74, v74
	v_exp_f32_e32 v75, v75
	v_mul_f32_e64 v76, |v68|, s84
	v_mul_f32_e64 v77, |v69|, s84
	v_add_f32_e32 v74, 1.0, v74
	v_add_f32_e32 v75, 1.0, v75
	v_log_f32_e32 v74, v74
	v_log_f32_e32 v75, v75
	v_exp_f32_e32 v76, v76
	v_exp_f32_e32 v77, v77
	v_min_f32_e32 v67, 0, v67
	v_min_f32_e32 v66, 0, v66
	v_pk_fma_f32 v[66:67], v[74:75], s[66:67], v[66:67] op_sel_hi:[1,0,1] neg_lo:[1,0,0] neg_hi:[1,0,0]
	v_add_f32_e32 v74, 1.0, v76
	v_add_f32_e32 v75, 1.0, v77
	v_log_f32_e32 v74, v74
	v_log_f32_e32 v75, v75
	v_min_f32_e32 v69, 0, v69
	v_min_f32_e32 v68, 0, v68
	v_lshlrev_b32_e32 v98, 2, v78
	v_pk_fma_f32 v[68:69], v[74:75], s[66:67], v[68:69] op_sel_hi:[1,0,1] neg_lo:[1,0,0] neg_hi:[1,0,0]
	v_add_u32_e32 v74, -2, v228
	v_cmp_lt_i32_e32 vcc, v74, v82
	v_cndmask_b32_e32 v74, v74, v228, vcc
	v_lshlrev_b32_e32 v99, 2, v74
	v_add_u32_e32 v74, -4, v228
	v_cmp_lt_i32_e32 vcc, v74, v82
	v_cndmask_b32_e32 v74, v74, v228, vcc
	v_lshlrev_b32_e32 v100, 2, v74
	v_add_u32_e32 v74, -8, v228
	v_cmp_lt_i32_e32 vcc, v74, v82
	v_cndmask_b32_e32 v74, v74, v228, vcc
	v_lshlrev_b32_e32 v101, 2, v74
	v_pk_mul_f32 v[66:67], v[66:67], s[68:69] op_sel_hi:[1,0]
	v_pk_mul_f32 v[68:69], v[68:69], s[68:69] op_sel_hi:[1,0]
	s_nop 1
	v_add_f32_dpp v66, v66, v66 row_shr:1 row_mask:0xf bank_mask:0xf
	v_add_f32_dpp v67, v67, v67 row_shr:1 row_mask:0xf bank_mask:0xf
	v_add_f32_dpp v68, v68, v68 row_shr:1 row_mask:0xf bank_mask:0xf
	v_add_f32_dpp v69, v69, v69 row_shr:1 row_mask:0xf bank_mask:0xf
	v_add_f32_dpp v66, v66, v66 row_shr:2 row_mask:0xf bank_mask:0xf
	v_add_f32_dpp v67, v67, v67 row_shr:2 row_mask:0xf bank_mask:0xf
	v_add_f32_dpp v68, v68, v68 row_shr:2 row_mask:0xf bank_mask:0xf
	v_add_f32_dpp v69, v69, v69 row_shr:2 row_mask:0xf bank_mask:0xf
	v_add_f32_dpp v66, v66, v66 row_shr:4 row_mask:0xf bank_mask:0xf
	v_add_f32_dpp v67, v67, v67 row_shr:4 row_mask:0xf bank_mask:0xf
	v_add_f32_dpp v68, v68, v68 row_shr:4 row_mask:0xf bank_mask:0xf
	v_add_f32_dpp v69, v69, v69 row_shr:4 row_mask:0xf bank_mask:0xf
	v_add_f32_dpp v66, v66, v66 row_shr:8 row_mask:0xf bank_mask:0xf
	v_add_f32_dpp v67, v67, v67 row_shr:8 row_mask:0xf bank_mask:0xf
	v_add_f32_dpp v68, v68, v68 row_shr:8 row_mask:0xf bank_mask:0xf
	v_add_f32_dpp v69, v69, v69 row_shr:8 row_mask:0xf bank_mask:0xf
	s_and_saveexec_b64 s[16:17], s[6:7]
	v_add_u32_e32 v74, s3, v107
	ds_write_b128 v74, v[66:69] offset:8192
	s_or_b64 exec, exec, s[16:17]
	v_mfma_f32_16x16x32_bf16 v[74:77], v[6:9], v[70:73], 0
	s_nop 7
	v_pk_add_f32 v[74:75], v[14:15], v[74:75]
	v_pk_add_f32 v[76:77], v[16:17], v[76:77]
	v_mul_f32_e64 v78, |v74|, s84
	v_mul_f32_e64 v79, |v75|, s84
	v_exp_f32_e32 v78, v78
	v_exp_f32_e32 v79, v79
	v_mul_f32_e64 v80, |v76|, s84
	v_mul_f32_e64 v81, |v77|, s84
	v_add_f32_e32 v78, 1.0, v78
	v_add_f32_e32 v79, 1.0, v79
	v_log_f32_e32 v78, v78
	v_log_f32_e32 v79, v79
	v_exp_f32_e32 v80, v80
	v_exp_f32_e32 v81, v81
	v_min_f32_e32 v75, 0, v75
	v_min_f32_e32 v74, 0, v74
	v_pk_fma_f32 v[74:75], v[78:79], s[66:67], v[74:75] op_sel_hi:[1,0,1] neg_lo:[1,0,0] neg_hi:[1,0,0]
	v_add_f32_e32 v78, 1.0, v80
	v_add_f32_e32 v79, 1.0, v81
	v_log_f32_e32 v78, v78
	v_log_f32_e32 v79, v79
	v_min_f32_e32 v77, 0, v77
	v_min_f32_e32 v76, 0, v76
	v_pk_fma_f32 v[76:77], v[78:79], s[66:67], v[76:77] op_sel_hi:[1,0,1] neg_lo:[1,0,0] neg_hi:[1,0,0]
	v_pk_mul_f32 v[74:75], v[74:75], s[68:69] op_sel_hi:[1,0]
	v_pk_mul_f32 v[76:77], v[76:77], s[68:69] op_sel_hi:[1,0]
	s_nop 1
	v_add_f32_dpp v74, v74, v74 row_shr:1 row_mask:0xf bank_mask:0xf
	v_add_f32_dpp v75, v75, v75 row_shr:1 row_mask:0xf bank_mask:0xf
	v_add_f32_dpp v76, v76, v76 row_shr:1 row_mask:0xf bank_mask:0xf
	v_add_f32_dpp v77, v77, v77 row_shr:1 row_mask:0xf bank_mask:0xf
	v_add_f32_dpp v74, v74, v74 row_shr:2 row_mask:0xf bank_mask:0xf
	v_add_f32_dpp v75, v75, v75 row_shr:2 row_mask:0xf bank_mask:0xf
	v_add_f32_dpp v76, v76, v76 row_shr:2 row_mask:0xf bank_mask:0xf
	v_add_f32_dpp v77, v77, v77 row_shr:2 row_mask:0xf bank_mask:0xf
	v_add_f32_dpp v74, v74, v74 row_shr:4 row_mask:0xf bank_mask:0xf
	v_add_f32_dpp v75, v75, v75 row_shr:4 row_mask:0xf bank_mask:0xf
	v_add_f32_dpp v76, v76, v76 row_shr:4 row_mask:0xf bank_mask:0xf
	v_add_f32_dpp v77, v77, v77 row_shr:4 row_mask:0xf bank_mask:0xf
	v_add_f32_dpp v74, v74, v74 row_shr:8 row_mask:0xf bank_mask:0xf
	v_add_f32_dpp v75, v75, v75 row_shr:8 row_mask:0xf bank_mask:0xf
	v_add_f32_dpp v76, v76, v76 row_shr:8 row_mask:0xf bank_mask:0xf
	v_add_f32_dpp v77, v77, v77 row_shr:8 row_mask:0xf bank_mask:0xf
	s_and_saveexec_b64 s[16:17], s[6:7]
	v_add_u32_e32 v78, s56, v107
	ds_write_b128 v78, v[74:77] offset:8192
	s_or_b64 exec, exec, s[16:17]
	v_mfma_f32_16x16x32_bf16 v[78:81], v[18:21], v[70:73], 0
	s_nop 7
	v_pk_add_f32 v[78:79], v[26:27], v[78:79]
	v_pk_add_f32 v[80:81], v[28:29], v[80:81]
	v_mul_f32_e64 v82, |v78|, s84
	v_mul_f32_e64 v83, |v79|, s84
	v_exp_f32_e32 v82, v82
	v_exp_f32_e32 v83, v83
	v_mul_f32_e64 v84, |v80|, s84
	v_mul_f32_e64 v85, |v81|, s84
	v_add_f32_e32 v82, 1.0, v82
	v_add_f32_e32 v83, 1.0, v83
	v_log_f32_e32 v82, v82
	v_log_f32_e32 v83, v83
	v_exp_f32_e32 v84, v84
	v_exp_f32_e32 v85, v85
	v_min_f32_e32 v79, 0, v79
	v_min_f32_e32 v78, 0, v78
	v_pk_fma_f32 v[78:79], v[82:83], s[66:67], v[78:79] op_sel_hi:[1,0,1] neg_lo:[1,0,0] neg_hi:[1,0,0]
; #define MFMA16(a, b, c) __builtin_amdgcn_mfma_f32_16x16x32_bf16((a), (b), (c), 0, 0, 0)
; __device__ __forceinline__ float logsig16(float x) { return ((x < 0.f ? x : 0.f) - 0.6931471805599453f * __builtin_amdgcn_logf(1.0f + __builtin_amdgcn_exp2f(-1.4426950408889634f * fabsf(x)))) * (1.0f / 16.0f); }
; template <int layer> __device__ __forceinline__ void layer_phases(const Ctx& c, unsigned char* lds) {
;     ...
;                     for (int ct = 0; ct < 8; ++ct) { const f32x4 z = MFMA16(wfr[ct], afr, ((f32x4){0.f, 0.f, 0.f, 0.f})) + bcl[ct];
;                         f32x4 v; v[0] = pg8::logsig16(z[0]); v[1] = pg8::logsig16(z[1]); v[2] = pg8::logsig16(z[2]); v[3] = pg8::logsig16(z[3]);
; #pragma unroll
;                         for (int st = 1; st < 16; st <<= 1) { f32x4 t;
; #pragma unroll
;                             for (int j = 0; j < 4; ++j) t[j] = __shfl_up(v[j], st, 16);
;                             if (ql >= st) v += t; }
;                         cv[ct] = v;
;                         if (ql == 15) *(f32x4*)(tot + rt * 256 + 16 * (8 * kh + ct) + 4 * g4) = v; }
	v_add_f32_e32 v82, 1.0, v84
	v_add_f32_e32 v83, 1.0, v85
	v_log_f32_e32 v82, v82
	v_log_f32_e32 v83, v83
	v_min_f32_e32 v81, 0, v81
	v_min_f32_e32 v80, 0, v80
	v_pk_fma_f32 v[80:81], v[82:83], s[66:67], v[80:81] op_sel_hi:[1,0,1] neg_lo:[1,0,0] neg_hi:[1,0,0]
	v_pk_mul_f32 v[78:79], v[78:79], s[68:69] op_sel_hi:[1,0]
	v_pk_mul_f32 v[80:81], v[80:81], s[68:69] op_sel_hi:[1,0]
	s_nop 1
	v_add_f32_dpp v78, v78, v78 row_shr:1 row_mask:0xf bank_mask:0xf
	v_add_f32_dpp v79, v79, v79 row_shr:1 row_mask:0xf bank_mask:0xf
	v_add_f32_dpp v80, v80, v80 row_shr:1 row_mask:0xf bank_mask:0xf
	v_add_f32_dpp v81, v81, v81 row_shr:1 row_mask:0xf bank_mask:0xf
	v_add_f32_dpp v78, v78, v78 row_shr:2 row_mask:0xf bank_mask:0xf
	v_add_f32_dpp v79, v79, v79 row_shr:2 row_mask:0xf bank_mask:0xf
	v_add_f32_dpp v80, v80, v80 row_shr:2 row_mask:0xf bank_mask:0xf
	v_add_f32_dpp v81, v81, v81 row_shr:2 row_mask:0xf bank_mask:0xf
	v_add_f32_dpp v78, v78, v78 row_shr:4 row_mask:0xf bank_mask:0xf
	v_add_f32_dpp v79, v79, v79 row_shr:4 row_mask:0xf bank_mask:0xf
	v_add_f32_dpp v80, v80, v80 row_shr:4 row_mask:0xf bank_mask:0xf
	v_add_f32_dpp v81, v81, v81 row_shr:4 row_mask:0xf bank_mask:0xf
	v_add_f32_dpp v78, v78, v78 row_shr:8 row_mask:0xf bank_mask:0xf
	v_add_f32_dpp v79, v79, v79 row_shr:8 row_mask:0xf bank_mask:0xf
	v_add_f32_dpp v80, v80, v80 row_shr:8 row_mask:0xf bank_mask:0xf
	v_add_f32_dpp v81, v81, v81 row_shr:8 row_mask:0xf bank_mask:0xf
	s_and_saveexec_b64 s[16:17], s[6:7]
	v_add_u32_e32 v82, s57, v107
	ds_write_b128 v82, v[78:81] offset:8192
	s_or_b64 exec, exec, s[16:17]
	v_mfma_f32_16x16x32_bf16 v[82:85], v[22:25], v[70:73], 0
	s_nop 7
	v_pk_add_f32 v[82:83], v[30:31], v[82:83]
	v_pk_add_f32 v[84:85], v[32:33], v[84:85]
	v_mul_f32_e64 v86, |v82|, s84
	v_mul_f32_e64 v87, |v83|, s84
	v_exp_f32_e32 v86, v86
	v_exp_f32_e32 v87, v87
	v_mul_f32_e64 v88, |v84|, s84
	v_mul_f32_e64 v89, |v85|, s84
	v_add_f32_e32 v86, 1.0, v86
	v_add_f32_e32 v87, 1.0, v87
	v_log_f32_e32 v86, v86
	v_log_f32_e32 v87, v87
	v_exp_f32_e32 v88, v88
	v_exp_f32_e32 v89, v89
	v_min_f32_e32 v83, 0, v83
	v_min_f32_e32 v82, 0, v82
	v_pk_fma_f32 v[82:83], v[86:87], s[66:67], v[82:83] op_sel_hi:[1,0,1] neg_lo:[1,0,0] neg_hi:[1,0,0]
	v_add_f32_e32 v86, 1.0, v88
	v_add_f32_e32 v87, 1.0, v89
	v_log_f32_e32 v86, v86
	v_log_f32_e32 v87, v87
	v_min_f32_e32 v85, 0, v85
	v_min_f32_e32 v84, 0, v84
	v_pk_fma_f32 v[84:85], v[86:87], s[66:67], v[84:85] op_sel_hi:[1,0,1] neg_lo:[1,0,0] neg_hi:[1,0,0]
	v_pk_mul_f32 v[82:83], v[82:83], s[68:69] op_sel_hi:[1,0]
	v_pk_mul_f32 v[84:85], v[84:85], s[68:69] op_sel_hi:[1,0]
	s_nop 1
	v_add_f32_dpp v82, v82, v82 row_shr:1 row_mask:0xf bank_mask:0xf
	v_add_f32_dpp v83, v83, v83 row_shr:1 row_mask:0xf bank_mask:0xf
	v_add_f32_dpp v84, v84, v84 row_shr:1 row_mask:0xf bank_mask:0xf
	v_add_f32_dpp v85, v85, v85 row_shr:1 row_mask:0xf bank_mask:0xf
	v_add_f32_dpp v82, v82, v82 row_shr:2 row_mask:0xf bank_mask:0xf
	v_add_f32_dpp v83, v83, v83 row_shr:2 row_mask:0xf bank_mask:0xf
	v_add_f32_dpp v84, v84, v84 row_shr:2 row_mask:0xf bank_mask:0xf
	v_add_f32_dpp v85, v85, v85 row_shr:2 row_mask:0xf bank_mask:0xf
	v_add_f32_dpp v82, v82, v82 row_shr:4 row_mask:0xf bank_mask:0xf
	v_add_f32_dpp v83, v83, v83 row_shr:4 row_mask:0xf bank_mask:0xf
	v_add_f32_dpp v84, v84, v84 row_shr:4 row_mask:0xf bank_mask:0xf
	v_add_f32_dpp v85, v85, v85 row_shr:4 row_mask:0xf bank_mask:0xf
	v_add_f32_dpp v82, v82, v82 row_shr:8 row_mask:0xf bank_mask:0xf
	v_add_f32_dpp v83, v83, v83 row_shr:8 row_mask:0xf bank_mask:0xf
	v_add_f32_dpp v84, v84, v84 row_shr:8 row_mask:0xf bank_mask:0xf
	v_add_f32_dpp v85, v85, v85 row_shr:8 row_mask:0xf bank_mask:0xf
	s_and_saveexec_b64 s[16:17], s[6:7]
	v_add_u32_e32 v86, s67, v107
	ds_write_b128 v86, v[82:85] offset:8192
	s_or_b64 exec, exec, s[16:17]
	v_mfma_f32_16x16x32_bf16 v[86:89], v[34:37], v[70:73], 0
	s_nop 7
	v_pk_add_f32 v[86:87], v[42:43], v[86:87]
	v_pk_add_f32 v[88:89], v[44:45], v[88:89]
	v_mul_f32_e64 v90, |v86|, s84
	v_mul_f32_e64 v91, |v87|, s84
	v_exp_f32_e32 v90, v90
	v_exp_f32_e32 v91, v91
	v_mul_f32_e64 v92, |v88|, s84
	v_mul_f32_e64 v93, |v89|, s84
	v_add_f32_e32 v90, 1.0, v90
	v_add_f32_e32 v91, 1.0, v91
	v_log_f32_e32 v90, v90
	v_log_f32_e32 v91, v91
	v_exp_f32_e32 v92, v92
	v_exp_f32_e32 v93, v93
	v_min_f32_e32 v87, 0, v87
	v_min_f32_e32 v86, 0, v86
	v_pk_fma_f32 v[86:87], v[90:91], s[66:67], v[86:87] op_sel_hi:[1,0,1] neg_lo:[1,0,0] neg_hi:[1,0,0]
	v_add_f32_e32 v90, 1.0, v92
	v_add_f32_e32 v91, 1.0, v93
	v_log_f32_e32 v90, v90
	v_log_f32_e32 v91, v91
	v_min_f32_e32 v89, 0, v89
	v_min_f32_e32 v88, 0, v88
	v_pk_fma_f32 v[88:89], v[90:91], s[66:67], v[88:89] op_sel_hi:[1,0,1] neg_lo:[1,0,0] neg_hi:[1,0,0]
	v_pk_mul_f32 v[86:87], v[86:87], s[68:69] op_sel_hi:[1,0]
	v_pk_mul_f32 v[88:89], v[88:89], s[68:69] op_sel_hi:[1,0]
	s_nop 1
	v_add_f32_dpp v86, v86, v86 row_shr:1 row_mask:0xf bank_mask:0xf
	v_add_f32_dpp v87, v87, v87 row_shr:1 row_mask:0xf bank_mask:0xf
	v_add_f32_dpp v88, v88, v88 row_shr:1 row_mask:0xf bank_mask:0xf
	v_add_f32_dpp v89, v89, v89 row_shr:1 row_mask:0xf bank_mask:0xf
	v_add_f32_dpp v86, v86, v86 row_shr:2 row_mask:0xf bank_mask:0xf
	v_add_f32_dpp v87, v87, v87 row_shr:2 row_mask:0xf bank_mask:0xf
	v_add_f32_dpp v88, v88, v88 row_shr:2 row_mask:0xf bank_mask:0xf
	v_add_f32_dpp v89, v89, v89 row_shr:2 row_mask:0xf bank_mask:0xf
	v_add_f32_dpp v86, v86, v86 row_shr:4 row_mask:0xf bank_mask:0xf
	v_add_f32_dpp v87, v87, v87 row_shr:4 row_mask:0xf bank_mask:0xf
	v_add_f32_dpp v88, v88, v88 row_shr:4 row_mask:0xf bank_mask:0xf
	v_add_f32_dpp v89, v89, v89 row_shr:4 row_mask:0xf bank_mask:0xf
; #define MFMA16(a, b, c) __builtin_amdgcn_mfma_f32_16x16x32_bf16((a), (b), (c), 0, 0, 0)
; __device__ __forceinline__ float logsig16(float x) { return ((x < 0.f ? x : 0.f) - 0.6931471805599453f * __builtin_amdgcn_logf(1.0f + __builtin_amdgcn_exp2f(-1.4426950408889634f * fabsf(x)))) * (1.0f / 16.0f); }
; template <int layer> __device__ __forceinline__ void layer_phases(const Ctx& c, unsigned char* lds) {
;     ...
;                     for (int ct = 0; ct < 8; ++ct) { const f32x4 z = MFMA16(wfr[ct], afr, ((f32x4){0.f, 0.f, 0.f, 0.f})) + bcl[ct];
;                         f32x4 v; v[0] = pg8::logsig16(z[0]); v[1] = pg8::logsig16(z[1]); v[2] = pg8::logsig16(z[2]); v[3] = pg8::logsig16(z[3]);
; #pragma unroll
;                         for (int st = 1; st < 16; st <<= 1) { f32x4 t;
; #pragma unroll
;                             for (int j = 0; j < 4; ++j) t[j] = __shfl_up(v[j], st, 16);
;                             if (ql >= st) v += t; }
;                         cv[ct] = v;
;                         if (ql == 15) *(f32x4*)(tot + rt * 256 + 16 * (8 * kh + ct) + 4 * g4) = v; }
	v_add_f32_dpp v86, v86, v86 row_shr:8 row_mask:0xf bank_mask:0xf
	v_add_f32_dpp v87, v87, v87 row_shr:8 row_mask:0xf bank_mask:0xf
	v_add_f32_dpp v88, v88, v88 row_shr:8 row_mask:0xf bank_mask:0xf
	v_add_f32_dpp v89, v89, v89 row_shr:8 row_mask:0xf bank_mask:0xf
	s_and_saveexec_b64 s[16:17], s[6:7]
	v_add_u32_e32 v90, s69, v107
	ds_write_b128 v90, v[86:89] offset:8192
	s_or_b64 exec, exec, s[16:17]
	v_mfma_f32_16x16x32_bf16 v[90:93], v[38:41], v[70:73], 0
	s_nop 7
	v_pk_add_f32 v[90:91], v[46:47], v[90:91]
	v_pk_add_f32 v[92:93], v[48:49], v[92:93]
	v_mul_f32_e64 v94, |v90|, s84
	v_mul_f32_e64 v95, |v91|, s84
	v_exp_f32_e32 v94, v94
	v_exp_f32_e32 v95, v95
	v_mul_f32_e64 v96, |v92|, s84
	v_mul_f32_e64 v97, |v93|, s84
	v_add_f32_e32 v94, 1.0, v94
	v_add_f32_e32 v95, 1.0, v95
	v_log_f32_e32 v94, v94
	v_log_f32_e32 v95, v95
	v_exp_f32_e32 v96, v96
	v_exp_f32_e32 v97, v97
	v_min_f32_e32 v91, 0, v91
	v_min_f32_e32 v90, 0, v90
	v_pk_fma_f32 v[90:91], v[94:95], s[66:67], v[90:91] op_sel_hi:[1,0,1] neg_lo:[1,0,0] neg_hi:[1,0,0]
	v_add_f32_e32 v94, 1.0, v96
	v_add_f32_e32 v95, 1.0, v97
	v_log_f32_e32 v94, v94
	v_log_f32_e32 v95, v95
	v_min_f32_e32 v93, 0, v93
	v_min_f32_e32 v92, 0, v92
	v_pk_fma_f32 v[92:93], v[94:95], s[66:67], v[92:93] op_sel_hi:[1,0,1] neg_lo:[1,0,0] neg_hi:[1,0,0]
	v_pk_mul_f32 v[90:91], v[90:91], s[68:69] op_sel_hi:[1,0]
	v_pk_mul_f32 v[92:93], v[92:93], s[68:69] op_sel_hi:[1,0]
	s_nop 1
	v_add_f32_dpp v90, v90, v90 row_shr:1 row_mask:0xf bank_mask:0xf
	v_add_f32_dpp v91, v91, v91 row_shr:1 row_mask:0xf bank_mask:0xf
	v_add_f32_dpp v92, v92, v92 row_shr:1 row_mask:0xf bank_mask:0xf
	v_add_f32_dpp v93, v93, v93 row_shr:1 row_mask:0xf bank_mask:0xf
	v_add_f32_dpp v90, v90, v90 row_shr:2 row_mask:0xf bank_mask:0xf
	v_add_f32_dpp v91, v91, v91 row_shr:2 row_mask:0xf bank_mask:0xf
	v_add_f32_dpp v92, v92, v92 row_shr:2 row_mask:0xf bank_mask:0xf
	v_add_f32_dpp v93, v93, v93 row_shr:2 row_mask:0xf bank_mask:0xf
	v_add_f32_dpp v90, v90, v90 row_shr:4 row_mask:0xf bank_mask:0xf
	v_add_f32_dpp v91, v91, v91 row_shr:4 row_mask:0xf bank_mask:0xf
	v_add_f32_dpp v92, v92, v92 row_shr:4 row_mask:0xf bank_mask:0xf
	v_add_f32_dpp v93, v93, v93 row_shr:4 row_mask:0xf bank_mask:0xf
	v_add_f32_dpp v90, v90, v90 row_shr:8 row_mask:0xf bank_mask:0xf
	v_add_f32_dpp v91, v91, v91 row_shr:8 row_mask:0xf bank_mask:0xf
	v_add_f32_dpp v92, v92, v92 row_shr:8 row_mask:0xf bank_mask:0xf
	v_add_f32_dpp v93, v93, v93 row_shr:8 row_mask:0xf bank_mask:0xf
	s_and_saveexec_b64 s[16:17], s[6:7]
	v_add_u32_e32 v94, s80, v107
	ds_write_b128 v94, v[90:93] offset:8192
	s_or_b64 exec, exec, s[16:17]
	v_mfma_f32_16x16x32_bf16 v[94:97], v[50:53], v[70:73], 0
	s_nop 7
	v_pk_add_f32 v[94:95], v[58:59], v[94:95]
	v_pk_add_f32 v[96:97], v[60:61], v[96:97]
	v_mul_f32_e64 v102, |v94|, s84
	v_mul_f32_e64 v103, |v95|, s84
	v_exp_f32_e32 v102, v102
	v_exp_f32_e32 v103, v103
	v_mul_f32_e64 v104, |v96|, s84
	v_mul_f32_e64 v105, |v97|, s84
	v_add_f32_e32 v102, 1.0, v102
	v_add_f32_e32 v103, 1.0, v103
	v_log_f32_e32 v102, v102
	v_log_f32_e32 v103, v103
	v_exp_f32_e32 v104, v104
	v_exp_f32_e32 v105, v105
	v_min_f32_e32 v95, 0, v95
	v_min_f32_e32 v94, 0, v94
	v_pk_fma_f32 v[94:95], v[102:103], s[66:67], v[94:95] op_sel_hi:[1,0,1] neg_lo:[1,0,0] neg_hi:[1,0,0]
	v_add_f32_e32 v102, 1.0, v104
	v_add_f32_e32 v103, 1.0, v105
	v_log_f32_e32 v102, v102
	v_log_f32_e32 v103, v103
	v_min_f32_e32 v97, 0, v97
	v_min_f32_e32 v96, 0, v96
	v_pk_fma_f32 v[96:97], v[102:103], s[66:67], v[96:97] op_sel_hi:[1,0,1] neg_lo:[1,0,0] neg_hi:[1,0,0]
	v_pk_mul_f32 v[94:95], v[94:95], s[68:69] op_sel_hi:[1,0]
	v_pk_mul_f32 v[96:97], v[96:97], s[68:69] op_sel_hi:[1,0]
	s_nop 1
	v_add_f32_dpp v94, v94, v94 row_shr:1 row_mask:0xf bank_mask:0xf
; __device__ __forceinline__ float logsig16(float x) { return ((x < 0.f ? x : 0.f) - 0.6931471805599453f * __builtin_amdgcn_logf(1.0f + __builtin_amdgcn_exp2f(-1.4426950408889634f * fabsf(x)))) * (1.0f / 16.0f); }
; #define MFMA16(a, b, c) __builtin_amdgcn_mfma_f32_16x16x32_bf16((a), (b), (c), 0, 0, 0)
; template <int layer> __device__ __forceinline__ void layer_phases(const Ctx& c, unsigned char* lds) {
;     ...
;                     for (int ct = 0; ct < 8; ++ct) { const f32x4 z = MFMA16(wfr[ct], afr, ((f32x4){0.f, 0.f, 0.f, 0.f})) + bcl[ct];
;                         f32x4 v; v[0] = pg8::logsig16(z[0]); v[1] = pg8::logsig16(z[1]); v[2] = pg8::logsig16(z[2]); v[3] = pg8::logsig16(z[3]);
; #pragma unroll
;                         for (int st = 1; st < 16; st <<= 1) { f32x4 t;
; #pragma unroll
;                             for (int j = 0; j < 4; ++j) t[j] = __shfl_up(v[j], st, 16);
;                             if (ql >= st) v += t; }
;                         cv[ct] = v;
;                         if (ql == 15) *(f32x4*)(tot + rt * 256 + 16 * (8 * kh + ct) + 4 * g4) = v; }
;                     __syncthreads();
; #pragma unroll
;                     for (int ct = 0; ct < 8; ++ct) { f32x4 v = cv[ct];
; #pragma unroll
;                         for (int r2 = 0; r2 < 3; ++r2) if (r2 < rt) v += *(const f32x4*)(tot + r2 * 256 + 16 * (8 * kh + ct) + 4 * g4);
	v_add_f32_dpp v95, v95, v95 row_shr:1 row_mask:0xf bank_mask:0xf
	v_add_f32_dpp v96, v96, v96 row_shr:1 row_mask:0xf bank_mask:0xf
	v_add_f32_dpp v97, v97, v97 row_shr:1 row_mask:0xf bank_mask:0xf
	v_add_f32_dpp v94, v94, v94 row_shr:2 row_mask:0xf bank_mask:0xf
	v_add_f32_dpp v95, v95, v95 row_shr:2 row_mask:0xf bank_mask:0xf
	v_add_f32_dpp v96, v96, v96 row_shr:2 row_mask:0xf bank_mask:0xf
	v_add_f32_dpp v97, v97, v97 row_shr:2 row_mask:0xf bank_mask:0xf
	v_add_f32_dpp v94, v94, v94 row_shr:4 row_mask:0xf bank_mask:0xf
	v_add_f32_dpp v95, v95, v95 row_shr:4 row_mask:0xf bank_mask:0xf
	v_add_f32_dpp v96, v96, v96 row_shr:4 row_mask:0xf bank_mask:0xf
	v_add_f32_dpp v97, v97, v97 row_shr:4 row_mask:0xf bank_mask:0xf
	v_add_f32_dpp v94, v94, v94 row_shr:8 row_mask:0xf bank_mask:0xf
	v_add_f32_dpp v95, v95, v95 row_shr:8 row_mask:0xf bank_mask:0xf
	v_add_f32_dpp v96, v96, v96 row_shr:8 row_mask:0xf bank_mask:0xf
	v_add_f32_dpp v97, v97, v97 row_shr:8 row_mask:0xf bank_mask:0xf
	s_and_saveexec_b64 s[16:17], s[6:7]
	v_add_u32_e32 v102, s81, v107
	ds_write_b128 v102, v[94:97] offset:8192
	s_or_b64 exec, exec, s[16:17]
	v_mfma_f32_16x16x32_bf16 v[70:73], v[54:57], v[70:73], 0
	s_nop 7
	v_pk_add_f32 v[70:71], v[62:63], v[70:71]
	v_pk_add_f32 v[72:73], v[64:65], v[72:73]
	v_mul_f32_e64 v102, |v70|, s84
	v_mul_f32_e64 v103, |v71|, s84
	v_exp_f32_e32 v102, v102
	v_exp_f32_e32 v103, v103
	v_mul_f32_e64 v104, |v72|, s84
	v_mul_f32_e64 v105, |v73|, s84
	v_add_f32_e32 v102, 1.0, v102
	v_add_f32_e32 v103, 1.0, v103
	v_log_f32_e32 v102, v102
	v_log_f32_e32 v103, v103
	v_exp_f32_e32 v104, v104
	v_exp_f32_e32 v105, v105
	v_min_f32_e32 v71, 0, v71
	v_min_f32_e32 v70, 0, v70
	v_pk_fma_f32 v[70:71], v[102:103], s[66:67], v[70:71] op_sel_hi:[1,0,1] neg_lo:[1,0,0] neg_hi:[1,0,0]
	v_add_f32_e32 v102, 1.0, v104
	v_add_f32_e32 v103, 1.0, v105
	v_log_f32_e32 v102, v102
	v_log_f32_e32 v103, v103
	v_min_f32_e32 v73, 0, v73
	v_min_f32_e32 v72, 0, v72
	v_pk_fma_f32 v[72:73], v[102:103], s[66:67], v[72:73] op_sel_hi:[1,0,1] neg_lo:[1,0,0] neg_hi:[1,0,0]
	v_pk_mul_f32 v[70:71], v[70:71], s[68:69] op_sel_hi:[1,0]
	v_pk_mul_f32 v[72:73], v[72:73], s[68:69] op_sel_hi:[1,0]
	s_nop 1
	v_add_f32_dpp v70, v70, v70 row_shr:1 row_mask:0xf bank_mask:0xf
	v_add_f32_dpp v71, v71, v71 row_shr:1 row_mask:0xf bank_mask:0xf
	v_add_f32_dpp v72, v72, v72 row_shr:1 row_mask:0xf bank_mask:0xf
	v_add_f32_dpp v73, v73, v73 row_shr:1 row_mask:0xf bank_mask:0xf
	v_add_f32_dpp v70, v70, v70 row_shr:2 row_mask:0xf bank_mask:0xf
	v_add_f32_dpp v71, v71, v71 row_shr:2 row_mask:0xf bank_mask:0xf
	v_add_f32_dpp v72, v72, v72 row_shr:2 row_mask:0xf bank_mask:0xf
	v_add_f32_dpp v73, v73, v73 row_shr:2 row_mask:0xf bank_mask:0xf
	v_add_f32_dpp v70, v70, v70 row_shr:4 row_mask:0xf bank_mask:0xf
	v_add_f32_dpp v71, v71, v71 row_shr:4 row_mask:0xf bank_mask:0xf
	v_add_f32_dpp v72, v72, v72 row_shr:4 row_mask:0xf bank_mask:0xf
	v_add_f32_dpp v73, v73, v73 row_shr:4 row_mask:0xf bank_mask:0xf
	v_add_f32_dpp v70, v70, v70 row_shr:8 row_mask:0xf bank_mask:0xf
	v_add_f32_dpp v71, v71, v71 row_shr:8 row_mask:0xf bank_mask:0xf
	v_add_f32_dpp v72, v72, v72 row_shr:8 row_mask:0xf bank_mask:0xf
	v_add_f32_dpp v73, v73, v73 row_shr:8 row_mask:0xf bank_mask:0xf
	s_and_saveexec_b64 s[16:17], s[6:7]
	v_add_u32_e32 v98, s82, v107
	ds_write_b128 v98, v[70:73] offset:8192
	s_or_b64 exec, exec, s[16:17]
	v_cndmask_b32_e64 v98, 0, 1, s[58:59]
	v_cmp_ne_u32_e64 s[16:17], 1, v98
	s_andn2_b64 vcc, exec, s[58:59]
	v_add_u32_e32 v98, s3, v144
	s_waitcnt lgkmcnt(0)
	s_barrier
	s_cbranch_vccnz .LBB0_978
	ds_read_b128 v[100:103], v98 offset:8192
	s_waitcnt lgkmcnt(0)
	v_pk_add_f32 v[68:69], v[68:69], v[102:103]
	v_pk_add_f32 v[66:67], v[66:67], v[100:101]
